# gdnprep stage A (wave 0 only, seven waves wait behind it): the two small-array loads of the next unit requested one unit ahead into free registers
# speedup vs baseline: 1.0018x; 1.0018x over previous
; DI void gdn_prep_unit(const Params& p, int U, char* lds) {
;     ...
;   __syncthreads();
; DI void phase_gdnprep(const Params& p, int bid, int nb, char* lds) {
;   for (int U = bid; U < 2048; U += nb) gdn_prep_unit(p, U, lds);
.LBB0_1086:
	s_or_b64 exec, exec, s[4:5]
	s_movk_i32 s2, 0x800
	v_cmp_gt_i32_e64 s[4:5], s2, v176
	s_and_saveexec_b64 s[16:17], s[4:5]
	s_cbranch_execz .LBB0_1155
	s_mov_b32 s6, 0
	s_add_u32 s26, s66, 0x2000000
	s_addc_u32 s27, s67, 0
	s_add_u32 s28, s66, 0x4000000
	s_addc_u32 s29, s67, 0
	s_add_u32 s30, s84, 0x1a00000
	s_addc_u32 s31, s85, 0
	s_add_u32 s34, s84, 0x1e000000
	s_addc_u32 s35, s85, 0
	v_add_u32_e32 v0, 0, v190
	v_mbcnt_hi_u32_b32 v123, -1, v177
	s_add_u32 s38, s84, 0x1c000000
	v_add_u32_e32 v26, 0xcc00, v0
	v_add_u32_e32 v28, 0xee00, v0
	v_add_u32_e32 v111, 0x2080, v0
	v_add_u32_e32 v117, 0x80, v0
	v_and_b32_e32 v165, 64, v123
	s_mov_b32 s0, 0x358637bd
	v_bfrev_b32_e32 v0, 0.5
	v_add_u32_e32 v29, 0x11400, v146
	v_add_u32_e32 v105, 0x11800, v146
	s_addc_u32 s39, s85, 0
	s_mov_b64 s[40:41], 0
	v_mov_b32_e32 v30, 0
	s_movk_i32 s3, 0x2c00
	v_xor_b32_e32 v164, 4, v123
	v_add_u32_e32 v166, 64, v165
	s_mov_b32 s42, 0x3db504f3
	s_movk_i32 s18, 0x110
	s_mov_b32 s19, 0x800000
	s_movk_i32 s22, 0x88
	s_mov_b32 s23, 0x5040100
	s_movk_i32 s43, 0x440
	s_movk_i32 s68, 0x48
	s_movk_i32 s69, 0x90
	s_movk_i32 s72, 0x7ff
	v_add_u32_e32 v167, -1, v123
	v_add_u32_e32 v168, -2, v123
	v_add_u32_e32 v169, -4, v123
	v_add_u32_e32 v170, -8, v123
	v_add_u32_e32 v171, -16, v123
	v_subrev_u32_e32 v172, 32, v123
	v_lshl_or_b32 v173, v123, 2, v0
	v_mov_b64_e32 v[32:33], s[0:1]
	v_mov_b32_e32 v174, 0x1100
	v_mov_b32_e32 v34, v176
	s_branch .LBB0_1089

; DI void gdn_prep_unit(const Params& p, int U, char* lds) {
;     ...
;   if (wid == 0) {
;     const float g = small[(t0 + lane) * 16 + 12 + h], bt = small[(t0 + lane) * 16 + 8 + h];
;     float cs = g;
; #pragma unroll
;     for (int d = 1; d < 64; d <<= 1) { const float n = __shfl_up(cs, d); if (lane >= d) cs += n; }
;     const float gl = __shfl(cs, 63);
;     gcs[lane] = cs; gcs[64 + lane] = bt; gcs[128 + lane] = __expf(cs); gcs[192 + lane] = __expf(gl - cs);
;     if (lane == 0) { gcs[256] = __expf(gl); ((float*)(p.ws + WS_GL))[U] = __expf(gl); }
;   }
.LBB0_1089:
	v_ashrrev_i32_e32 v0, 9, v34
	v_mov_b32_e32 v175, v206
	s_waitcnt lgkmcnt(1)
	v_ashrrev_i32_e32 v1, 31, v0
	s_waitcnt lgkmcnt(0)
	v_lshlrev_b32_e32 v3, 6, v34
	v_lshlrev_b64 v[0:1], 13, v[0:1]
	v_and_b32_e32 v178, 63, v175
	v_and_b32_e32 v3, 0x1fc0, v3
	v_bfe_u32 v2, v34, 7, 2
	v_or_b32_e32 v0, v0, v3
	v_ashrrev_i32_e32 v35, 31, v34
	v_cmp_gt_u32_e32 vcc, 64, v175
	v_lshl_add_u32 v179, v178, 2, v29
	s_barrier
	s_and_saveexec_b64 s[8:9], vcc
	s_cbranch_execz .LBB0_1092
	v_or_b32_e32 v4, v0, v175
	v_mov_b32_e32 v5, v1
	v_lshlrev_b64 v[4:5], 6, v[4:5]
	v_lshl_add_u64 v[4:5], s[24:25], 0, v[4:5]
	v_lshlrev_b32_e32 v6, 2, v2
	v_mov_b32_e32 v7, v30
	v_lshl_add_u64 v[4:5], v[4:5], 0, v[6:7]
	v_add_co_u32_e32 v246, vcc, 0x80000, v4
	s_nop 1
	v_addc_co_u32_e32 v247, vcc, 0, v5, vcc
	s_cmp_eq_u32 s6, 0
	s_cbranch_scc0 .Lga_pref
	global_load_dword v6, v[4:5], off offset:48
	s_nop 0
	global_load_dword v5, v[4:5], off offset:32
	s_branch .Lga_join
.Lga_pref:
	v_mov_b32_e32 v6, v244
	v_mov_b32_e32 v5, v245
.Lga_join:
	global_load_dword v244, v[246:247], off offset:48
	global_load_dword v245, v[246:247], off offset:32
	s_mov_b32 s6, 1
	v_cmp_lt_i32_e32 vcc, v167, v165
	v_cmp_lt_i32_e64 s[0:1], v169, v165
	s_nop 0
	v_cndmask_b32_e32 v4, v167, v123, vcc
	v_lshlrev_b32_e32 v4, 2, v4
	v_cmp_lt_i32_e32 vcc, v168, v165
	s_waitcnt vmcnt(3)
	ds_bpermute_b32 v4, v4, v6
	v_cndmask_b32_e32 v7, v168, v123, vcc
	v_cmp_eq_u32_e32 vcc, 0, v178
	v_lshlrev_b32_e32 v7, 2, v7
	s_waitcnt lgkmcnt(0)
	v_add_f32_e32 v4, v6, v4
	v_cndmask_b32_e32 v4, v4, v6, vcc
	ds_bpermute_b32 v6, v7, v4
	v_cndmask_b32_e64 v7, v169, v123, s[0:1]
	v_cmp_gt_u32_e64 s[0:1], 2, v178
	v_lshlrev_b32_e32 v7, 2, v7
	s_waitcnt lgkmcnt(0)
	v_add_f32_e32 v6, v4, v6
	v_cndmask_b32_e64 v4, v6, v4, s[0:1]
	ds_bpermute_b32 v6, v7, v4
	v_cmp_lt_i32_e64 s[0:1], v170, v165
	s_waitcnt lgkmcnt(0)
	v_add_f32_e32 v6, v4, v6
	v_cndmask_b32_e64 v7, v170, v123, s[0:1]
	v_cmp_gt_u32_e64 s[0:1], 4, v178
	v_lshlrev_b32_e32 v7, 2, v7
	s_nop 0
	v_cndmask_b32_e64 v4, v6, v4, s[0:1]
	ds_bpermute_b32 v6, v7, v4
	v_cmp_lt_i32_e64 s[0:1], v171, v165
	s_waitcnt lgkmcnt(0)
	v_add_f32_e32 v6, v4, v6
	v_cndmask_b32_e64 v7, v171, v123, s[0:1]
	v_cmp_gt_u32_e64 s[0:1], 8, v178
	v_lshlrev_b32_e32 v7, 2, v7
	s_nop 0
	v_cndmask_b32_e64 v4, v6, v4, s[0:1]
	ds_bpermute_b32 v6, v7, v4
	v_cmp_lt_i32_e64 s[0:1], v172, v165
	s_waitcnt lgkmcnt(0)
	v_add_f32_e32 v6, v4, v6
	v_cndmask_b32_e64 v7, v172, v123, s[0:1]
	v_cmp_gt_u32_e64 s[0:1], 16, v178
	v_lshlrev_b32_e32 v7, 2, v7
	s_nop 0
	v_cndmask_b32_e64 v4, v6, v4, s[0:1]
	ds_bpermute_b32 v6, v7, v4
	v_cmp_gt_u32_e64 s[0:1], 32, v178
	s_waitcnt lgkmcnt(0)
	v_add_f32_e32 v6, v4, v6
	v_cndmask_b32_e64 v6, v6, v4, s[0:1]
	ds_bpermute_b32 v4, v173, v6
	v_mul_f32_e32 v7, 0x3fb8aa3b, v6
	v_exp_f32_e32 v7, v7
	ds_write_b32 v179, v6
	s_waitcnt lgkmcnt(1)
	v_sub_f32_e32 v8, v4, v6
	v_mul_f32_e32 v8, 0x3fb8aa3b, v8
	v_exp_f32_e32 v8, v8
	v_lshl_add_u32 v6, v175, 2, v29
	s_waitcnt vmcnt(2)
	ds_write2st64_b32 v6, v5, v7 offset0:1 offset1:2
	ds_write_b32 v6, v8 offset:768
	s_and_b64 exec, exec, vcc
	s_cbranch_execz .LBB0_1092
	v_mul_f32_e32 v4, 0x3fb8aa3b, v4
	v_exp_f32_e32 v6, v4
	v_lshl_add_u64 v[4:5], v[34:35], 2, s[30:31]
	ds_write_b32 v105, v6
	global_store_dword v[4:5], v6, off
